# cross-attention QK^T body: the 64 key-fragment LDS reads (one per MFMA) were requested one MFMA ahead; same reads and MFMAs with seven fragments in flight
# baseline (speedup 1.0000x reference)
; #define MFMA16(b, a, c) __builtin_amdgcn_mfma_f32_16x16x32_bf16((b), (a), (c), 0, 0, 0)
; __device__ __forceinline__ void xattn_unit(LAS unsigned char* lds, int hd, int qt, const bf16_t* QX, const bf16_t* KX, const bf16_t* VX, bf16_t* O) {
;     ...
; #pragma unroll
;         for (int ks = 0; ks < 4; ++ks)
; #pragma unroll
;             for (int j = 0; j < 16; ++j) S[j] = MFMA16(row_frag(X, (128 + 8) * 2, 16 * j, 32 * ks, lane), aq[ks], S[j]);
.LBB0_979:
	s_waitcnt lgkmcnt(0)
	s_barrier
	s_add_u32 s10, s10, 0x100
	s_addc_u32 s11, s11, 0
	s_cmpk_lg_i32 s10, 0x400
	ds_read_b128 v[210:213], v200
	ds_read_b128 v[214:217], v200 offset:4352
	ds_read_b128 v[228:231], v200 offset:8704
	ds_read_b128 v[232:235], v200 offset:13056
	ds_read_b128 v[236:239], v200 offset:17408
	ds_read_b128 v[240:243], v200 offset:21760
	ds_read_b128 v[244:247], v200 offset:26112
	s_waitcnt lgkmcnt(6)
	s_waitcnt vmcnt(11)
	v_mfma_f32_16x16x32_bf16 v[94:97], v[210:213], v[110:113], v[94:97]
	ds_read_b128 v[210:213], v200 offset:30464
	s_waitcnt lgkmcnt(6)
	v_mfma_f32_16x16x32_bf16 v[90:93], v[214:217], v[110:113], v[90:93]
	ds_read_b128 v[214:217], v200 offset:34816
	s_waitcnt lgkmcnt(6)
	v_mfma_f32_16x16x32_bf16 v[86:89], v[228:231], v[110:113], v[86:89]
	ds_read_b128 v[228:231], v200 offset:39168
	s_waitcnt lgkmcnt(6)
	v_mfma_f32_16x16x32_bf16 v[82:85], v[232:235], v[110:113], v[82:85]
	ds_read_b128 v[232:235], v200 offset:43520
	s_waitcnt lgkmcnt(6)
	v_mfma_f32_16x16x32_bf16 v[78:81], v[236:239], v[110:113], v[78:81]
	ds_read_b128 v[236:239], v200 offset:47872
	s_waitcnt lgkmcnt(6)
	v_mfma_f32_16x16x32_bf16 v[74:77], v[240:243], v[110:113], v[74:77]
	ds_read_b128 v[240:243], v200 offset:52224
	s_waitcnt lgkmcnt(6)
	v_mfma_f32_16x16x32_bf16 v[70:73], v[244:247], v[110:113], v[70:73]
	ds_read_b128 v[244:247], v200 offset:56576
	s_waitcnt lgkmcnt(6)
	v_mfma_f32_16x16x32_bf16 v[66:69], v[210:213], v[110:113], v[66:69]
	ds_read_b128 v[210:213], v200 offset:60928
	s_waitcnt lgkmcnt(6)
	v_mfma_f32_16x16x32_bf16 v[62:65], v[214:217], v[110:113], v[62:65]
	ds_read_b128 v[214:217], v200 offset:65280
	s_waitcnt lgkmcnt(6)
	v_mfma_f32_16x16x32_bf16 v[58:61], v[228:231], v[110:113], v[58:61]
	ds_read_b128 v[228:231], v200 offset:64
	s_waitcnt lgkmcnt(6)
	v_mfma_f32_16x16x32_bf16 v[54:57], v[232:235], v[110:113], v[54:57]
	ds_read_b128 v[232:235], v200 offset:4416
	s_waitcnt lgkmcnt(6)
	v_mfma_f32_16x16x32_bf16 v[50:53], v[236:239], v[110:113], v[50:53]
	ds_read_b128 v[236:239], v200 offset:8768
	s_waitcnt lgkmcnt(6)
	v_mfma_f32_16x16x32_bf16 v[46:49], v[240:243], v[110:113], v[46:49]
	ds_read_b128 v[240:243], v200 offset:13120
	s_waitcnt lgkmcnt(6)
	v_mfma_f32_16x16x32_bf16 v[42:45], v[244:247], v[110:113], v[42:45]
	ds_read_b128 v[244:247], v200 offset:17472
	s_waitcnt lgkmcnt(6)
	v_mfma_f32_16x16x32_bf16 v[38:41], v[210:213], v[110:113], v[38:41]
	ds_read_b128 v[210:213], v200 offset:21824
	s_waitcnt lgkmcnt(6)
	v_mfma_f32_16x16x32_bf16 v[34:37], v[214:217], v[110:113], v[34:37]
	ds_read_b128 v[214:217], v200 offset:26176
	s_waitcnt lgkmcnt(6)
	s_waitcnt vmcnt(10)
	v_mfma_f32_16x16x32_bf16 v[94:97], v[228:231], v[106:109], v[94:97]
	ds_read_b128 v[228:231], v200 offset:30528
	s_waitcnt lgkmcnt(6)
	v_mfma_f32_16x16x32_bf16 v[90:93], v[232:235], v[106:109], v[90:93]
	ds_read_b128 v[232:235], v200 offset:34880
	s_waitcnt lgkmcnt(6)
	v_mfma_f32_16x16x32_bf16 v[86:89], v[236:239], v[106:109], v[86:89]
	ds_read_b128 v[236:239], v200 offset:39232
	s_waitcnt lgkmcnt(6)
	v_mfma_f32_16x16x32_bf16 v[82:85], v[240:243], v[106:109], v[82:85]
	ds_read_b128 v[240:243], v200 offset:43584
	s_waitcnt lgkmcnt(6)
	v_mfma_f32_16x16x32_bf16 v[78:81], v[244:247], v[106:109], v[78:81]
	ds_read_b128 v[244:247], v200 offset:47936
	s_waitcnt lgkmcnt(6)
	v_mfma_f32_16x16x32_bf16 v[74:77], v[210:213], v[106:109], v[74:77]
	ds_read_b128 v[210:213], v200 offset:52288
	s_waitcnt lgkmcnt(6)
	v_mfma_f32_16x16x32_bf16 v[70:73], v[214:217], v[106:109], v[70:73]
	ds_read_b128 v[214:217], v200 offset:56640
	s_waitcnt lgkmcnt(6)
	v_mfma_f32_16x16x32_bf16 v[66:69], v[228:231], v[106:109], v[66:69]
	ds_read_b128 v[228:231], v200 offset:60992
	s_waitcnt lgkmcnt(6)
	v_mfma_f32_16x16x32_bf16 v[62:65], v[232:235], v[106:109], v[62:65]
	ds_read_b128 v[232:235], v200 offset:65344
	s_waitcnt lgkmcnt(6)
	v_mfma_f32_16x16x32_bf16 v[58:61], v[236:239], v[106:109], v[58:61]
	ds_read_b128 v[236:239], v200 offset:128
	s_waitcnt lgkmcnt(6)
	v_mfma_f32_16x16x32_bf16 v[54:57], v[240:243], v[106:109], v[54:57]
	ds_read_b128 v[240:243], v200 offset:4480
	s_waitcnt lgkmcnt(6)
	v_mfma_f32_16x16x32_bf16 v[50:53], v[244:247], v[106:109], v[50:53]
	ds_read_b128 v[244:247], v200 offset:8832
	s_waitcnt lgkmcnt(6)
	v_mfma_f32_16x16x32_bf16 v[46:49], v[210:213], v[106:109], v[46:49]
	ds_read_b128 v[210:213], v200 offset:13184
	s_waitcnt lgkmcnt(6)
; #define MFMA16(b, a, c) __builtin_amdgcn_mfma_f32_16x16x32_bf16((b), (a), (c), 0, 0, 0)
; __device__ __forceinline__ void xattn_unit(LAS unsigned char* lds, int hd, int qt, const bf16_t* QX, const bf16_t* KX, const bf16_t* VX, bf16_t* O) {
;     ...
; #pragma unroll
;         for (int ks = 0; ks < 4; ++ks)
; #pragma unroll
;             for (int j = 0; j < 16; ++j) S[j] = MFMA16(row_frag(X, (128 + 8) * 2, 16 * j, 32 * ks, lane), aq[ks], S[j]);
	v_mfma_f32_16x16x32_bf16 v[42:45], v[214:217], v[106:109], v[42:45]
	ds_read_b128 v[214:217], v200 offset:17536
	s_waitcnt lgkmcnt(6)
	v_mfma_f32_16x16x32_bf16 v[38:41], v[228:231], v[106:109], v[38:41]
	ds_read_b128 v[228:231], v200 offset:21888
	s_waitcnt lgkmcnt(6)
	v_mfma_f32_16x16x32_bf16 v[34:37], v[232:235], v[106:109], v[34:37]
	ds_read_b128 v[232:235], v200 offset:26240
	s_waitcnt lgkmcnt(6)
	s_waitcnt vmcnt(9)
	v_mfma_f32_16x16x32_bf16 v[94:97], v[236:239], v[102:105], v[94:97]
	ds_read_b128 v[236:239], v200 offset:30592
	s_waitcnt lgkmcnt(6)
	v_mfma_f32_16x16x32_bf16 v[90:93], v[240:243], v[102:105], v[90:93]
	ds_read_b128 v[240:243], v200 offset:34944
	s_waitcnt lgkmcnt(6)
	v_mfma_f32_16x16x32_bf16 v[86:89], v[244:247], v[102:105], v[86:89]
	ds_read_b128 v[244:247], v200 offset:39296
	s_waitcnt lgkmcnt(6)
	v_mfma_f32_16x16x32_bf16 v[82:85], v[210:213], v[102:105], v[82:85]
	ds_read_b128 v[210:213], v200 offset:43648
	s_waitcnt lgkmcnt(6)
	v_mfma_f32_16x16x32_bf16 v[78:81], v[214:217], v[102:105], v[78:81]
	ds_read_b128 v[214:217], v200 offset:48000
	s_waitcnt lgkmcnt(6)
	v_mfma_f32_16x16x32_bf16 v[74:77], v[228:231], v[102:105], v[74:77]
	ds_read_b128 v[228:231], v200 offset:52352
	s_waitcnt lgkmcnt(6)
	v_mfma_f32_16x16x32_bf16 v[70:73], v[232:235], v[102:105], v[70:73]
	ds_read_b128 v[232:235], v200 offset:56704
	s_waitcnt lgkmcnt(6)
	v_mfma_f32_16x16x32_bf16 v[66:69], v[236:239], v[102:105], v[66:69]
	ds_read_b128 v[236:239], v200 offset:61056
	s_waitcnt lgkmcnt(6)
	v_mfma_f32_16x16x32_bf16 v[62:65], v[240:243], v[102:105], v[62:65]
	ds_read_b128 v[240:243], v200 offset:65408
	s_waitcnt lgkmcnt(6)
	v_mfma_f32_16x16x32_bf16 v[58:61], v[244:247], v[102:105], v[58:61]
	ds_read_b128 v[244:247], v200 offset:192
	s_waitcnt lgkmcnt(6)
	v_mfma_f32_16x16x32_bf16 v[54:57], v[210:213], v[102:105], v[54:57]
	ds_read_b128 v[210:213], v200 offset:4544
	s_waitcnt lgkmcnt(6)
	v_mfma_f32_16x16x32_bf16 v[50:53], v[214:217], v[102:105], v[50:53]
	ds_read_b128 v[214:217], v200 offset:8896
	s_waitcnt lgkmcnt(6)
	v_mfma_f32_16x16x32_bf16 v[46:49], v[228:231], v[102:105], v[46:49]
	ds_read_b128 v[228:231], v200 offset:13248
	s_waitcnt lgkmcnt(6)
	v_mfma_f32_16x16x32_bf16 v[42:45], v[232:235], v[102:105], v[42:45]
	ds_read_b128 v[232:235], v200 offset:17600
	s_waitcnt lgkmcnt(6)
	v_mfma_f32_16x16x32_bf16 v[38:41], v[236:239], v[102:105], v[38:41]
	ds_read_b128 v[236:239], v200 offset:21952
	s_waitcnt lgkmcnt(6)
	v_mfma_f32_16x16x32_bf16 v[34:37], v[240:243], v[102:105], v[34:37]
	ds_read_b128 v[240:243], v200 offset:26304
	s_waitcnt lgkmcnt(6)
	s_waitcnt vmcnt(8)
	v_mfma_f32_16x16x32_bf16 v[94:97], v[244:247], v[98:101], v[94:97]
	ds_read_b128 v[244:247], v200 offset:30656
	s_waitcnt lgkmcnt(6)
	v_mfma_f32_16x16x32_bf16 v[90:93], v[210:213], v[98:101], v[90:93]
	ds_read_b128 v[210:213], v200 offset:35008
	s_waitcnt lgkmcnt(6)
	v_mfma_f32_16x16x32_bf16 v[86:89], v[214:217], v[98:101], v[86:89]
	ds_read_b128 v[214:217], v200 offset:39360
	s_waitcnt lgkmcnt(6)
	v_mfma_f32_16x16x32_bf16 v[82:85], v[228:231], v[98:101], v[82:85]
	ds_read_b128 v[228:231], v200 offset:43712
	s_waitcnt lgkmcnt(6)
	v_mfma_f32_16x16x32_bf16 v[78:81], v[232:235], v[98:101], v[78:81]
	ds_read_b128 v[232:235], v200 offset:48064
	s_waitcnt lgkmcnt(6)
	v_mfma_f32_16x16x32_bf16 v[74:77], v[236:239], v[98:101], v[74:77]
	ds_read_b128 v[236:239], v200 offset:52416
	s_waitcnt lgkmcnt(6)
	v_mfma_f32_16x16x32_bf16 v[70:73], v[240:243], v[98:101], v[70:73]
	ds_read_b128 v[240:243], v200 offset:56768
	s_waitcnt lgkmcnt(6)
	v_mfma_f32_16x16x32_bf16 v[66:69], v[244:247], v[98:101], v[66:69]
	ds_read_b128 v[244:247], v200 offset:61120
	s_waitcnt lgkmcnt(6)
	v_mfma_f32_16x16x32_bf16 v[62:65], v[210:213], v[98:101], v[62:65]
	ds_read_b128 v[210:213], v200 offset:65472
	s_waitcnt lgkmcnt(6)
	v_mfma_f32_16x16x32_bf16 v[58:61], v[214:217], v[98:101], v[58:61]
	s_waitcnt lgkmcnt(5)
	v_mfma_f32_16x16x32_bf16 v[54:57], v[228:231], v[98:101], v[54:57]
	s_waitcnt lgkmcnt(4)
	v_mfma_f32_16x16x32_bf16 v[50:53], v[232:235], v[98:101], v[50:53]
	s_waitcnt lgkmcnt(3)
	v_mfma_f32_16x16x32_bf16 v[46:49], v[236:239], v[98:101], v[46:49]
	s_waitcnt lgkmcnt(2)
	v_mfma_f32_16x16x32_bf16 v[42:45], v[240:243], v[98:101], v[42:45]
	s_waitcnt lgkmcnt(1)
	v_mfma_f32_16x16x32_bf16 v[38:41], v[244:247], v[98:101], v[38:41]
	s_waitcnt lgkmcnt(0)
	v_mfma_f32_16x16x32_bf16 v[34:37], v[210:213], v[98:101], v[34:37]
	s_cbranch_scc0 .LBB0_982

; __device__ __forceinline__ void xattn_unit(LAS unsigned char* lds, int hd, int qt, const bf16_t* QX, const bf16_t* KX, const bf16_t* VX, bf16_t* O) {
;     ...
;         for (int ks = 0; ks < 4; ++ks) aq[ks] = *(const bf16x8*)(QX + trow * D + hd * XD + kc * 128 + 32 * ks + 8 * fq);
;         if (kc < 3) stage_load<NMEM, 128>(pf, KX + hd * XD + (kc + 1) * 128, D, tid);
.Lxa_last_0:
	global_load_dword v249, v[180:181], off
	global_load_dword v249, v[180:181], off
	global_load_dword v249, v[180:181], off
	global_load_dword v249, v[180:181], off
	global_load_dword v249, v[180:181], off
	global_load_dword v249, v[180:181], off
	global_load_dword v249, v[180:181], off
	global_load_dword v249, v[180:181], off
	s_branch .LBB0_979

; #define MFMA16(b, a, c) __builtin_amdgcn_mfma_f32_16x16x32_bf16((b), (a), (c), 0, 0, 0)
; __device__ __forceinline__ void xattn_unit(LAS unsigned char* lds, int hd, int qt, const bf16_t* QX, const bf16_t* KX, const bf16_t* VX, bf16_t* O) {
;     ...
; #pragma unroll
;         for (int ks = 0; ks < 4; ++ks)
; #pragma unroll
;             for (int j = 0; j < 16; ++j) S[j] = MFMA16(row_frag(X, (128 + 8) * 2, 16 * j, 32 * ks, lane), aq[ks], S[j]);
.LBB0_1814:
	s_waitcnt lgkmcnt(0)
	s_barrier
	s_add_u32 s12, s12, 0x100
	s_addc_u32 s13, s13, 0
	s_cmpk_lg_i32 s12, 0x400
	ds_read_b128 v[210:213], v200
	ds_read_b128 v[214:217], v200 offset:4352
	ds_read_b128 v[228:231], v200 offset:8704
	ds_read_b128 v[232:235], v200 offset:13056
	ds_read_b128 v[236:239], v200 offset:17408
	ds_read_b128 v[240:243], v200 offset:21760
	ds_read_b128 v[244:247], v200 offset:26112
	s_waitcnt lgkmcnt(6)
	s_waitcnt vmcnt(11)
	v_mfma_f32_16x16x32_bf16 v[94:97], v[210:213], v[110:113], v[94:97]
	ds_read_b128 v[210:213], v200 offset:30464
	s_waitcnt lgkmcnt(6)
	v_mfma_f32_16x16x32_bf16 v[90:93], v[214:217], v[110:113], v[90:93]
	ds_read_b128 v[214:217], v200 offset:34816
	s_waitcnt lgkmcnt(6)
	v_mfma_f32_16x16x32_bf16 v[86:89], v[228:231], v[110:113], v[86:89]
	ds_read_b128 v[228:231], v200 offset:39168
	s_waitcnt lgkmcnt(6)
	v_mfma_f32_16x16x32_bf16 v[82:85], v[232:235], v[110:113], v[82:85]
	ds_read_b128 v[232:235], v200 offset:43520
	s_waitcnt lgkmcnt(6)
	v_mfma_f32_16x16x32_bf16 v[78:81], v[236:239], v[110:113], v[78:81]
	ds_read_b128 v[236:239], v200 offset:47872
	s_waitcnt lgkmcnt(6)
	v_mfma_f32_16x16x32_bf16 v[74:77], v[240:243], v[110:113], v[74:77]
	ds_read_b128 v[240:243], v200 offset:52224
	s_waitcnt lgkmcnt(6)
	v_mfma_f32_16x16x32_bf16 v[70:73], v[244:247], v[110:113], v[70:73]
	ds_read_b128 v[244:247], v200 offset:56576
	s_waitcnt lgkmcnt(6)
	v_mfma_f32_16x16x32_bf16 v[66:69], v[210:213], v[110:113], v[66:69]
	ds_read_b128 v[210:213], v200 offset:60928
	s_waitcnt lgkmcnt(6)
	v_mfma_f32_16x16x32_bf16 v[62:65], v[214:217], v[110:113], v[62:65]
	ds_read_b128 v[214:217], v200 offset:65280
	s_waitcnt lgkmcnt(6)
	v_mfma_f32_16x16x32_bf16 v[58:61], v[228:231], v[110:113], v[58:61]
	ds_read_b128 v[228:231], v200 offset:64
	s_waitcnt lgkmcnt(6)
	v_mfma_f32_16x16x32_bf16 v[54:57], v[232:235], v[110:113], v[54:57]
	ds_read_b128 v[232:235], v200 offset:4416
	s_waitcnt lgkmcnt(6)
	v_mfma_f32_16x16x32_bf16 v[50:53], v[236:239], v[110:113], v[50:53]
	ds_read_b128 v[236:239], v200 offset:8768
	s_waitcnt lgkmcnt(6)
	v_mfma_f32_16x16x32_bf16 v[46:49], v[240:243], v[110:113], v[46:49]
	ds_read_b128 v[240:243], v200 offset:13120
	s_waitcnt lgkmcnt(6)
	v_mfma_f32_16x16x32_bf16 v[42:45], v[244:247], v[110:113], v[42:45]
	ds_read_b128 v[244:247], v200 offset:17472
	s_waitcnt lgkmcnt(6)
	v_mfma_f32_16x16x32_bf16 v[38:41], v[210:213], v[110:113], v[38:41]
	ds_read_b128 v[210:213], v200 offset:21824
	s_waitcnt lgkmcnt(6)
	v_mfma_f32_16x16x32_bf16 v[34:37], v[214:217], v[110:113], v[34:37]
	ds_read_b128 v[214:217], v200 offset:26176
	s_waitcnt lgkmcnt(6)
	s_waitcnt vmcnt(10)
	v_mfma_f32_16x16x32_bf16 v[94:97], v[228:231], v[106:109], v[94:97]
	ds_read_b128 v[228:231], v200 offset:30528
	s_waitcnt lgkmcnt(6)
	v_mfma_f32_16x16x32_bf16 v[90:93], v[232:235], v[106:109], v[90:93]
	ds_read_b128 v[232:235], v200 offset:34880
	s_waitcnt lgkmcnt(6)
	v_mfma_f32_16x16x32_bf16 v[86:89], v[236:239], v[106:109], v[86:89]
	ds_read_b128 v[236:239], v200 offset:39232
	s_waitcnt lgkmcnt(6)
	v_mfma_f32_16x16x32_bf16 v[82:85], v[240:243], v[106:109], v[82:85]
	ds_read_b128 v[240:243], v200 offset:43584
	s_waitcnt lgkmcnt(6)
	v_mfma_f32_16x16x32_bf16 v[78:81], v[244:247], v[106:109], v[78:81]
	ds_read_b128 v[244:247], v200 offset:47936
	s_waitcnt lgkmcnt(6)
	v_mfma_f32_16x16x32_bf16 v[74:77], v[210:213], v[106:109], v[74:77]
	ds_read_b128 v[210:213], v200 offset:52288
	s_waitcnt lgkmcnt(6)
	v_mfma_f32_16x16x32_bf16 v[70:73], v[214:217], v[106:109], v[70:73]
	ds_read_b128 v[214:217], v200 offset:56640
	s_waitcnt lgkmcnt(6)
	v_mfma_f32_16x16x32_bf16 v[66:69], v[228:231], v[106:109], v[66:69]
	ds_read_b128 v[228:231], v200 offset:60992
	s_waitcnt lgkmcnt(6)
	v_mfma_f32_16x16x32_bf16 v[62:65], v[232:235], v[106:109], v[62:65]
	ds_read_b128 v[232:235], v200 offset:65344
	s_waitcnt lgkmcnt(6)
	v_mfma_f32_16x16x32_bf16 v[58:61], v[236:239], v[106:109], v[58:61]
	ds_read_b128 v[236:239], v200 offset:128
	s_waitcnt lgkmcnt(6)
	v_mfma_f32_16x16x32_bf16 v[54:57], v[240:243], v[106:109], v[54:57]
	ds_read_b128 v[240:243], v200 offset:4480
	s_waitcnt lgkmcnt(6)
	v_mfma_f32_16x16x32_bf16 v[50:53], v[244:247], v[106:109], v[50:53]
	ds_read_b128 v[244:247], v200 offset:8832
	s_waitcnt lgkmcnt(6)
	v_mfma_f32_16x16x32_bf16 v[46:49], v[210:213], v[106:109], v[46:49]
	ds_read_b128 v[210:213], v200 offset:13184
	s_waitcnt lgkmcnt(6)
; #define MFMA16(b, a, c) __builtin_amdgcn_mfma_f32_16x16x32_bf16((b), (a), (c), 0, 0, 0)
; __device__ __forceinline__ void xattn_unit(LAS unsigned char* lds, int hd, int qt, const bf16_t* QX, const bf16_t* KX, const bf16_t* VX, bf16_t* O) {
;     ...
; #pragma unroll
;         for (int ks = 0; ks < 4; ++ks)
; #pragma unroll
;             for (int j = 0; j < 16; ++j) S[j] = MFMA16(row_frag(X, (128 + 8) * 2, 16 * j, 32 * ks, lane), aq[ks], S[j]);
	v_mfma_f32_16x16x32_bf16 v[42:45], v[214:217], v[106:109], v[42:45]
	ds_read_b128 v[214:217], v200 offset:17536
	s_waitcnt lgkmcnt(6)
	v_mfma_f32_16x16x32_bf16 v[38:41], v[228:231], v[106:109], v[38:41]
	ds_read_b128 v[228:231], v200 offset:21888
	s_waitcnt lgkmcnt(6)
	v_mfma_f32_16x16x32_bf16 v[34:37], v[232:235], v[106:109], v[34:37]
	ds_read_b128 v[232:235], v200 offset:26240
	s_waitcnt lgkmcnt(6)
	s_waitcnt vmcnt(9)
	v_mfma_f32_16x16x32_bf16 v[94:97], v[236:239], v[102:105], v[94:97]
	ds_read_b128 v[236:239], v200 offset:30592
	s_waitcnt lgkmcnt(6)
	v_mfma_f32_16x16x32_bf16 v[90:93], v[240:243], v[102:105], v[90:93]
	ds_read_b128 v[240:243], v200 offset:34944
	s_waitcnt lgkmcnt(6)
	v_mfma_f32_16x16x32_bf16 v[86:89], v[244:247], v[102:105], v[86:89]
	ds_read_b128 v[244:247], v200 offset:39296
	s_waitcnt lgkmcnt(6)
	v_mfma_f32_16x16x32_bf16 v[82:85], v[210:213], v[102:105], v[82:85]
	ds_read_b128 v[210:213], v200 offset:43648
	s_waitcnt lgkmcnt(6)
	v_mfma_f32_16x16x32_bf16 v[78:81], v[214:217], v[102:105], v[78:81]
	ds_read_b128 v[214:217], v200 offset:48000
	s_waitcnt lgkmcnt(6)
	v_mfma_f32_16x16x32_bf16 v[74:77], v[228:231], v[102:105], v[74:77]
	ds_read_b128 v[228:231], v200 offset:52352
	s_waitcnt lgkmcnt(6)
	v_mfma_f32_16x16x32_bf16 v[70:73], v[232:235], v[102:105], v[70:73]
	ds_read_b128 v[232:235], v200 offset:56704
	s_waitcnt lgkmcnt(6)
	v_mfma_f32_16x16x32_bf16 v[66:69], v[236:239], v[102:105], v[66:69]
	ds_read_b128 v[236:239], v200 offset:61056
	s_waitcnt lgkmcnt(6)
	v_mfma_f32_16x16x32_bf16 v[62:65], v[240:243], v[102:105], v[62:65]
	ds_read_b128 v[240:243], v200 offset:65408
	s_waitcnt lgkmcnt(6)
	v_mfma_f32_16x16x32_bf16 v[58:61], v[244:247], v[102:105], v[58:61]
	ds_read_b128 v[244:247], v200 offset:192
	s_waitcnt lgkmcnt(6)
	v_mfma_f32_16x16x32_bf16 v[54:57], v[210:213], v[102:105], v[54:57]
	ds_read_b128 v[210:213], v200 offset:4544
	s_waitcnt lgkmcnt(6)
	v_mfma_f32_16x16x32_bf16 v[50:53], v[214:217], v[102:105], v[50:53]
	ds_read_b128 v[214:217], v200 offset:8896
	s_waitcnt lgkmcnt(6)
	v_mfma_f32_16x16x32_bf16 v[46:49], v[228:231], v[102:105], v[46:49]
	ds_read_b128 v[228:231], v200 offset:13248
	s_waitcnt lgkmcnt(6)
	v_mfma_f32_16x16x32_bf16 v[42:45], v[232:235], v[102:105], v[42:45]
	ds_read_b128 v[232:235], v200 offset:17600
	s_waitcnt lgkmcnt(6)
	v_mfma_f32_16x16x32_bf16 v[38:41], v[236:239], v[102:105], v[38:41]
	ds_read_b128 v[236:239], v200 offset:21952
	s_waitcnt lgkmcnt(6)
	v_mfma_f32_16x16x32_bf16 v[34:37], v[240:243], v[102:105], v[34:37]
	ds_read_b128 v[240:243], v200 offset:26304
	s_waitcnt lgkmcnt(6)
	s_waitcnt vmcnt(8)
	v_mfma_f32_16x16x32_bf16 v[94:97], v[244:247], v[98:101], v[94:97]
	ds_read_b128 v[244:247], v200 offset:30656
	s_waitcnt lgkmcnt(6)
	v_mfma_f32_16x16x32_bf16 v[90:93], v[210:213], v[98:101], v[90:93]
	ds_read_b128 v[210:213], v200 offset:35008
	s_waitcnt lgkmcnt(6)
	v_mfma_f32_16x16x32_bf16 v[86:89], v[214:217], v[98:101], v[86:89]
	ds_read_b128 v[214:217], v200 offset:39360
	s_waitcnt lgkmcnt(6)
	v_mfma_f32_16x16x32_bf16 v[82:85], v[228:231], v[98:101], v[82:85]
	ds_read_b128 v[228:231], v200 offset:43712
	s_waitcnt lgkmcnt(6)
	v_mfma_f32_16x16x32_bf16 v[78:81], v[232:235], v[98:101], v[78:81]
	ds_read_b128 v[232:235], v200 offset:48064
	s_waitcnt lgkmcnt(6)
	v_mfma_f32_16x16x32_bf16 v[74:77], v[236:239], v[98:101], v[74:77]
	ds_read_b128 v[236:239], v200 offset:52416
	s_waitcnt lgkmcnt(6)
	v_mfma_f32_16x16x32_bf16 v[70:73], v[240:243], v[98:101], v[70:73]
	ds_read_b128 v[240:243], v200 offset:56768
	s_waitcnt lgkmcnt(6)
	v_mfma_f32_16x16x32_bf16 v[66:69], v[244:247], v[98:101], v[66:69]
	ds_read_b128 v[244:247], v200 offset:61120
	s_waitcnt lgkmcnt(6)
	v_mfma_f32_16x16x32_bf16 v[62:65], v[210:213], v[98:101], v[62:65]
	ds_read_b128 v[210:213], v200 offset:65472
	s_waitcnt lgkmcnt(6)
	v_mfma_f32_16x16x32_bf16 v[58:61], v[214:217], v[98:101], v[58:61]
	s_waitcnt lgkmcnt(5)
	v_mfma_f32_16x16x32_bf16 v[54:57], v[228:231], v[98:101], v[54:57]
	s_waitcnt lgkmcnt(4)
	v_mfma_f32_16x16x32_bf16 v[50:53], v[232:235], v[98:101], v[50:53]
	s_waitcnt lgkmcnt(3)
	v_mfma_f32_16x16x32_bf16 v[46:49], v[236:239], v[98:101], v[46:49]
	s_waitcnt lgkmcnt(2)
	v_mfma_f32_16x16x32_bf16 v[42:45], v[240:243], v[98:101], v[42:45]
	s_waitcnt lgkmcnt(1)
	v_mfma_f32_16x16x32_bf16 v[38:41], v[244:247], v[98:101], v[38:41]
	s_waitcnt lgkmcnt(0)
	v_mfma_f32_16x16x32_bf16 v[34:37], v[210:213], v[98:101], v[34:37]
	s_cbranch_scc0 .LBB0_1817
